# P1/P9/P10 set-up loops: all LDS-fill loads issued before one wait (were 8/4/16/8 serial round trips)
# baseline (speedup 1.0000x reference)
; #define LAS __attribute__((address_space(3)))
; __device__ __forceinline__ void p1_xn(const Args& a, const Frame& F) {
;     ...
;         for (int i = F.tid; i < 2 * 16 * 128; i += 512) { const int part = i >> 11, r = (i >> 7) & 15, c16 = i & 127;
;             *(LAS u32x4*)((part ? Wlo : Whi) + r * 2048 + ((c16 ^ r) << 4)) = *(const u32x4*)(wg + (size_t)part * 16384 + r * 1024 + c16 * 8); }
.LBB0_166:
	s_mov_b64 s[20:21], 0
	v_mov_b32_e32 v2, v152
	v_mov_b32_e32 v3, v0
	s_barrier
	v_lshrrev_b32_e32 v6, 11, v3
	v_and_b32_e32 v15, 15, v2
	v_lshlrev_b64 v[4:5], 15, v[6:7]
	v_lshlrev_b32_e32 v6, 11, v15
	v_lshl_add_u64 v[4:5], s[6:7], 0, v[4:5]
	v_lshl_add_u64 v[4:5], v[4:5], 0, v[6:7]
	v_lshl_add_u64 v[4:5], v[4:5], 0, v[12:13]
	global_load_dwordx4 v[176:179], v[4:5], off
	v_cmp_gt_u32_e32 vcc, s43, v3
	v_bitop3_b32 v5, v2, v146, 15 bitop3:0x6c
	v_add_u32_e32 v15, 0x200, v3
	v_cndmask_b32_e64 v4, v154, 0, vcc
	v_lshlrev_b32_e32 v5, 4, v5
	v_add_u32_e32 v2, 4, v2
	v_mov_b32_e32 v3, v15
	v_add3_u32 v208, v4, v6, v5
	v_lshrrev_b32_e32 v6, 11, v3
	v_and_b32_e32 v15, 15, v2
	v_lshlrev_b64 v[4:5], 15, v[6:7]
	v_lshlrev_b32_e32 v6, 11, v15
	v_lshl_add_u64 v[4:5], s[6:7], 0, v[4:5]
	v_lshl_add_u64 v[4:5], v[4:5], 0, v[6:7]
	v_lshl_add_u64 v[4:5], v[4:5], 0, v[12:13]
	global_load_dwordx4 v[180:183], v[4:5], off
	v_cmp_gt_u32_e32 vcc, s43, v3
	v_bitop3_b32 v5, v2, v146, 15 bitop3:0x6c
	v_add_u32_e32 v15, 0x200, v3
	v_cndmask_b32_e64 v4, v154, 0, vcc
	v_lshlrev_b32_e32 v5, 4, v5
	v_add_u32_e32 v2, 4, v2
	v_mov_b32_e32 v3, v15
	v_add3_u32 v209, v4, v6, v5
	v_lshrrev_b32_e32 v6, 11, v3
	v_and_b32_e32 v15, 15, v2
	v_lshlrev_b64 v[4:5], 15, v[6:7]
	v_lshlrev_b32_e32 v6, 11, v15
	v_lshl_add_u64 v[4:5], s[6:7], 0, v[4:5]
	v_lshl_add_u64 v[4:5], v[4:5], 0, v[6:7]
	v_lshl_add_u64 v[4:5], v[4:5], 0, v[12:13]
	global_load_dwordx4 v[184:187], v[4:5], off
	v_cmp_gt_u32_e32 vcc, s43, v3
	v_bitop3_b32 v5, v2, v146, 15 bitop3:0x6c
	v_add_u32_e32 v15, 0x200, v3
	v_cndmask_b32_e64 v4, v154, 0, vcc
	v_lshlrev_b32_e32 v5, 4, v5
	v_add_u32_e32 v2, 4, v2
	v_mov_b32_e32 v3, v15
	v_add3_u32 v210, v4, v6, v5
	v_lshrrev_b32_e32 v6, 11, v3
	v_and_b32_e32 v15, 15, v2
	v_lshlrev_b64 v[4:5], 15, v[6:7]
	v_lshlrev_b32_e32 v6, 11, v15
	v_lshl_add_u64 v[4:5], s[6:7], 0, v[4:5]
	v_lshl_add_u64 v[4:5], v[4:5], 0, v[6:7]
	v_lshl_add_u64 v[4:5], v[4:5], 0, v[12:13]
	global_load_dwordx4 v[188:191], v[4:5], off
	v_cmp_gt_u32_e32 vcc, s43, v3
	v_bitop3_b32 v5, v2, v146, 15 bitop3:0x6c
	v_add_u32_e32 v15, 0x200, v3
	v_cndmask_b32_e64 v4, v154, 0, vcc
	v_lshlrev_b32_e32 v5, 4, v5
	v_add_u32_e32 v2, 4, v2
	v_mov_b32_e32 v3, v15
	v_add3_u32 v211, v4, v6, v5
	v_lshrrev_b32_e32 v6, 11, v3
	v_and_b32_e32 v15, 15, v2
	v_lshlrev_b64 v[4:5], 15, v[6:7]
	v_lshlrev_b32_e32 v6, 11, v15
	v_lshl_add_u64 v[4:5], s[6:7], 0, v[4:5]
	v_lshl_add_u64 v[4:5], v[4:5], 0, v[6:7]
	v_lshl_add_u64 v[4:5], v[4:5], 0, v[12:13]
	global_load_dwordx4 v[192:195], v[4:5], off
	v_cmp_gt_u32_e32 vcc, s43, v3
	v_bitop3_b32 v5, v2, v146, 15 bitop3:0x6c
	v_add_u32_e32 v15, 0x200, v3
	v_cndmask_b32_e64 v4, v154, 0, vcc
	v_lshlrev_b32_e32 v5, 4, v5
	v_add_u32_e32 v2, 4, v2
	v_mov_b32_e32 v3, v15
	v_add3_u32 v212, v4, v6, v5
	v_lshrrev_b32_e32 v6, 11, v3
	v_and_b32_e32 v15, 15, v2
	v_lshlrev_b64 v[4:5], 15, v[6:7]
	v_lshlrev_b32_e32 v6, 11, v15
	v_lshl_add_u64 v[4:5], s[6:7], 0, v[4:5]
	v_lshl_add_u64 v[4:5], v[4:5], 0, v[6:7]
	v_lshl_add_u64 v[4:5], v[4:5], 0, v[12:13]
	global_load_dwordx4 v[196:199], v[4:5], off
	v_cmp_gt_u32_e32 vcc, s43, v3
	v_bitop3_b32 v5, v2, v146, 15 bitop3:0x6c
	v_add_u32_e32 v15, 0x200, v3
	v_cndmask_b32_e64 v4, v154, 0, vcc
	v_lshlrev_b32_e32 v5, 4, v5
	v_add_u32_e32 v2, 4, v2
	v_mov_b32_e32 v3, v15
	v_add3_u32 v213, v4, v6, v5
	v_lshrrev_b32_e32 v6, 11, v3
	v_and_b32_e32 v15, 15, v2
	v_lshlrev_b64 v[4:5], 15, v[6:7]
	v_lshlrev_b32_e32 v6, 11, v15
	v_lshl_add_u64 v[4:5], s[6:7], 0, v[4:5]
	v_lshl_add_u64 v[4:5], v[4:5], 0, v[6:7]
	v_lshl_add_u64 v[4:5], v[4:5], 0, v[12:13]
	global_load_dwordx4 v[200:203], v[4:5], off
	v_cmp_gt_u32_e32 vcc, s43, v3
	v_bitop3_b32 v5, v2, v146, 15 bitop3:0x6c
	v_add_u32_e32 v15, 0x200, v3
	v_cndmask_b32_e64 v4, v154, 0, vcc
	v_lshlrev_b32_e32 v5, 4, v5
	v_add_u32_e32 v2, 4, v2
	v_mov_b32_e32 v3, v15
	v_add3_u32 v214, v4, v6, v5
	v_lshrrev_b32_e32 v6, 11, v3
	v_and_b32_e32 v15, 15, v2
	v_lshlrev_b64 v[4:5], 15, v[6:7]
	v_lshlrev_b32_e32 v6, 11, v15
	v_lshl_add_u64 v[4:5], s[6:7], 0, v[4:5]
	v_lshl_add_u64 v[4:5], v[4:5], 0, v[6:7]
	v_lshl_add_u64 v[4:5], v[4:5], 0, v[12:13]
	global_load_dwordx4 v[204:207], v[4:5], off
	v_cmp_gt_u32_e32 vcc, s43, v3
	v_bitop3_b32 v5, v2, v146, 15 bitop3:0x6c
	v_add_u32_e32 v15, 0x200, v3
	v_cndmask_b32_e64 v4, v154, 0, vcc
	v_lshlrev_b32_e32 v5, 4, v5
	v_add_u32_e32 v2, 4, v2
	v_mov_b32_e32 v3, v15
	v_add3_u32 v215, v4, v6, v5
	s_waitcnt vmcnt(0)
; #define LAS __attribute__((address_space(3)))
; __device__ __forceinline__ void p1_xn(const Args& a, const Frame& F) {
;     ...
;             *(LAS u32x4*)((part ? Wlo : Whi) + r * 2048 + ((c16 ^ r) << 4)) = *(const u32x4*)(wg + (size_t)part * 16384 + r * 1024 + c16 * 8); }
;         for (int i = F.tid; i < 2 * 1024; i += 512) { const int mr = (i >> 10) ? 8 : mrb, k = i & 1023; NWS[i] = a.in[IN_N1W][k] * (1.0f + mod[mr * 6144 + 1024 + k]); SHV[i] = mod[mr * 6144 + k]; }
;         __syncthreads();
	ds_write_b128 v208, v[176:179]
	ds_write_b128 v209, v[180:183]
	ds_write_b128 v210, v[184:187]
	ds_write_b128 v211, v[188:191]
	ds_write_b128 v212, v[192:195]
	ds_write_b128 v213, v[196:199]
	ds_write_b128 v214, v[200:203]
	ds_write_b128 v215, v[204:207]
	s_or_b64 exec, exec, s[20:21]
	s_lshr_b32 s20, s50, 5
	s_mul_i32 s33, s20, 0x1800
	s_mov_b64 s[20:21], 0
	v_mov_b32_e32 v2, s33
	v_mov_b32_e32 v3, v153
	v_mov_b32_e32 v4, v0
	v_cmp_gt_u32_e32 vcc, s45, v4
	v_and_b32_e32 v5, 0x3ff, v4
	v_lshlrev_b32_e32 v15, 2, v5
	v_cndmask_b32_e32 v6, v155, v2, vcc
	v_or_b32_e32 v16, v6, v5
	v_ashrrev_i32_e32 v17, 31, v16
	v_lshl_add_u64 v[16:17], v[16:17], 2, s[8:9]
	v_add_co_u32_e32 v18, vcc, 0x1000, v16
	global_load_dword v176, v15, s[48:49]
	s_nop 0
	v_addc_co_u32_e32 v19, vcc, 0, v17, vcc
	global_load_dword v180, v[18:19], off
	global_load_dword v184, v[16:17], off
	v_add_u32_e32 v4, 0x200, v4
	v_cmp_gt_u32_e32 vcc, s45, v4
	v_and_b32_e32 v5, 0x3ff, v4
	v_lshlrev_b32_e32 v15, 2, v5
	v_cndmask_b32_e32 v6, v155, v2, vcc
	v_or_b32_e32 v16, v6, v5
	v_ashrrev_i32_e32 v17, 31, v16
	v_lshl_add_u64 v[16:17], v[16:17], 2, s[8:9]
	v_add_co_u32_e32 v18, vcc, 0x1000, v16
	global_load_dword v177, v15, s[48:49]
	s_nop 0
	v_addc_co_u32_e32 v19, vcc, 0, v17, vcc
	global_load_dword v181, v[18:19], off
	global_load_dword v185, v[16:17], off
	v_add_u32_e32 v4, 0x200, v4
	v_cmp_gt_u32_e32 vcc, s45, v4
	v_and_b32_e32 v5, 0x3ff, v4
	v_lshlrev_b32_e32 v15, 2, v5
	v_cndmask_b32_e32 v6, v155, v2, vcc
	v_or_b32_e32 v16, v6, v5
	v_ashrrev_i32_e32 v17, 31, v16
	v_lshl_add_u64 v[16:17], v[16:17], 2, s[8:9]
	v_add_co_u32_e32 v18, vcc, 0x1000, v16
	global_load_dword v178, v15, s[48:49]
	s_nop 0
	v_addc_co_u32_e32 v19, vcc, 0, v17, vcc
	global_load_dword v182, v[18:19], off
	global_load_dword v186, v[16:17], off
	v_add_u32_e32 v4, 0x200, v4
	v_cmp_gt_u32_e32 vcc, s45, v4
	v_and_b32_e32 v5, 0x3ff, v4
	v_lshlrev_b32_e32 v15, 2, v5
	v_cndmask_b32_e32 v6, v155, v2, vcc
	v_or_b32_e32 v16, v6, v5
	v_ashrrev_i32_e32 v17, 31, v16
	v_lshl_add_u64 v[16:17], v[16:17], 2, s[8:9]
	v_add_co_u32_e32 v18, vcc, 0x1000, v16
	global_load_dword v179, v15, s[48:49]
	s_nop 0
	v_addc_co_u32_e32 v19, vcc, 0, v17, vcc
	global_load_dword v183, v[18:19], off
	global_load_dword v187, v[16:17], off
	v_add_u32_e32 v4, 0x200, v4
	v_add_u32_e32 v16, 0xffffe000, v3
	s_waitcnt vmcnt(0)
	v_add_f32_e32 v6, 1.0, v180
	ds_write_b32 v3, v184
	v_mul_f32_e32 v5, v176, v6
	ds_write_b32 v16, v5
	v_add_f32_e32 v6, 1.0, v181
	ds_write_b32 v3, v185 offset:2048
	v_mul_f32_e32 v5, v177, v6
	ds_write_b32 v16, v5 offset:2048
	v_add_f32_e32 v6, 1.0, v182
	ds_write_b32 v3, v186 offset:4096
	v_mul_f32_e32 v5, v178, v6
	ds_write_b32 v16, v5 offset:4096
	v_add_f32_e32 v6, 1.0, v183
	ds_write_b32 v3, v187 offset:6144
	v_mul_f32_e32 v5, v179, v6
	ds_write_b32 v16, v5 offset:6144
	s_or_b64 exec, exec, s[20:21]
	s_cmp_lt_i32 s50, 32
	s_cselect_b32 s51, 20, 16
	s_lshl_b32 s58, s50, 2
	s_addk_i32 s58, 0x1000
	s_mov_b32 s59, 0
	s_waitcnt lgkmcnt(0)
	s_barrier
	s_branch .LBB0_172

; #define LAS __attribute__((address_space(3)))
; __device__ __forceinline__ void p9_router(const Args& a, const Frame& F) {
;     ...
;     __syncthreads();
;     for (int i = F.tid; i < 2 * 32 * 128; i += 512) { const int part = i >> 12, r = (i >> 7) & 31, c16 = i & 127;
;         *(LAS u32x4*)((part ? Wlo : Whi) + r * 2048 + ((c16 ^ (r & 15)) << 4)) = *(const u32x4*)(wr + (size_t)part * 32768 + r * 1024 + c16 * 8); }
.LBB0_806:
	s_cmp_lt_i32 s74, 10
	s_cselect_b64 s[4:5], -1, 0
	s_and_b64 s[20:21], s[4:5], s[0:1]
	s_andn2_b64 vcc, exec, s[20:21]
	s_cbranch_vccnz .LBB0_838
	s_add_u32 s0, s72, 0x1f00000
	v_and_b32_e32 v1, 0x7f, v0
	s_addc_u32 s1, s73, 0
	v_lshlrev_b32_e32 v2, 3, v1
	v_mov_b32_e32 v3, 0
	s_add_i32 s12, 0, 0x10000
	s_mov_b64 s[4:5], 0
	v_lshlrev_b32_e32 v4, 1, v2
	v_mov_b32_e32 v5, v3
	s_movk_i32 s6, 0x1000
	v_mov_b32_e32 v6, s12
	s_movk_i32 s7, 0x1dff
	v_mov_b32_e32 v7, v0
	s_waitcnt vmcnt(0) lgkmcnt(0)
	s_barrier
	v_lshrrev_b32_e32 v2, 12, v7
	v_lshlrev_b32_e32 v10, 11, v208
	v_lshlrev_b64 v[8:9], 16, v[2:3]
	v_and_b32_e32 v2, 0xf800, v10
	v_lshl_add_u64 v[8:9], s[0:1], 0, v[8:9]
	v_lshl_add_u64 v[8:9], v[8:9], 0, v[2:3]
	v_lshl_add_u64 v[8:9], v[8:9], 0, v[4:5]
	global_load_dwordx4 v[120:123], v[8:9], off
	v_cmp_gt_u32_e32 vcc, s6, v7
	v_bitop3_b32 v13, v208, v1, 15 bitop3:0x6c
	v_add_u32_e32 v14, 0x200, v7
	v_cndmask_b32_e64 v12, v6, 0, vcc
	v_lshlrev_b32_e32 v13, 4, v13
	v_add_u32_e32 v208, 4, v208
	v_mov_b32_e32 v7, v14
	v_add3_u32 v184, v12, v2, v13
	v_lshrrev_b32_e32 v2, 12, v7
	v_lshlrev_b32_e32 v10, 11, v208
	v_lshlrev_b64 v[8:9], 16, v[2:3]
	v_and_b32_e32 v2, 0xf800, v10
	v_lshl_add_u64 v[8:9], s[0:1], 0, v[8:9]
	v_lshl_add_u64 v[8:9], v[8:9], 0, v[2:3]
	v_lshl_add_u64 v[8:9], v[8:9], 0, v[4:5]
	global_load_dwordx4 v[124:127], v[8:9], off
	v_cmp_gt_u32_e32 vcc, s6, v7
	v_bitop3_b32 v13, v208, v1, 15 bitop3:0x6c
	v_add_u32_e32 v14, 0x200, v7
	v_cndmask_b32_e64 v12, v6, 0, vcc
	v_lshlrev_b32_e32 v13, 4, v13
	v_add_u32_e32 v208, 4, v208
	v_mov_b32_e32 v7, v14
	v_add3_u32 v185, v12, v2, v13
	v_lshrrev_b32_e32 v2, 12, v7
	v_lshlrev_b32_e32 v10, 11, v208
	v_lshlrev_b64 v[8:9], 16, v[2:3]
	v_and_b32_e32 v2, 0xf800, v10
	v_lshl_add_u64 v[8:9], s[0:1], 0, v[8:9]
	v_lshl_add_u64 v[8:9], v[8:9], 0, v[2:3]
	v_lshl_add_u64 v[8:9], v[8:9], 0, v[4:5]
	global_load_dwordx4 v[128:131], v[8:9], off
	v_cmp_gt_u32_e32 vcc, s6, v7
	v_bitop3_b32 v13, v208, v1, 15 bitop3:0x6c
	v_add_u32_e32 v14, 0x200, v7
	v_cndmask_b32_e64 v12, v6, 0, vcc
	v_lshlrev_b32_e32 v13, 4, v13
	v_add_u32_e32 v208, 4, v208
	v_mov_b32_e32 v7, v14
	v_add3_u32 v186, v12, v2, v13
	v_lshrrev_b32_e32 v2, 12, v7
	v_lshlrev_b32_e32 v10, 11, v208
	v_lshlrev_b64 v[8:9], 16, v[2:3]
	v_and_b32_e32 v2, 0xf800, v10
	v_lshl_add_u64 v[8:9], s[0:1], 0, v[8:9]
	v_lshl_add_u64 v[8:9], v[8:9], 0, v[2:3]
	v_lshl_add_u64 v[8:9], v[8:9], 0, v[4:5]
	global_load_dwordx4 v[132:135], v[8:9], off
	v_cmp_gt_u32_e32 vcc, s6, v7
	v_bitop3_b32 v13, v208, v1, 15 bitop3:0x6c
	v_add_u32_e32 v14, 0x200, v7
	v_cndmask_b32_e64 v12, v6, 0, vcc
	v_lshlrev_b32_e32 v13, 4, v13
	v_add_u32_e32 v208, 4, v208
	v_mov_b32_e32 v7, v14
	v_add3_u32 v187, v12, v2, v13
	v_lshrrev_b32_e32 v2, 12, v7
	v_lshlrev_b32_e32 v10, 11, v208
	v_lshlrev_b64 v[8:9], 16, v[2:3]
	v_and_b32_e32 v2, 0xf800, v10
	v_lshl_add_u64 v[8:9], s[0:1], 0, v[8:9]
	v_lshl_add_u64 v[8:9], v[8:9], 0, v[2:3]
	v_lshl_add_u64 v[8:9], v[8:9], 0, v[4:5]
	global_load_dwordx4 v[136:139], v[8:9], off
	v_cmp_gt_u32_e32 vcc, s6, v7
	v_bitop3_b32 v13, v208, v1, 15 bitop3:0x6c
	v_add_u32_e32 v14, 0x200, v7
	v_cndmask_b32_e64 v12, v6, 0, vcc
	v_lshlrev_b32_e32 v13, 4, v13
	v_add_u32_e32 v208, 4, v208
	v_mov_b32_e32 v7, v14
	v_add3_u32 v188, v12, v2, v13
	v_lshrrev_b32_e32 v2, 12, v7
	v_lshlrev_b32_e32 v10, 11, v208
	v_lshlrev_b64 v[8:9], 16, v[2:3]
	v_and_b32_e32 v2, 0xf800, v10
	v_lshl_add_u64 v[8:9], s[0:1], 0, v[8:9]
	v_lshl_add_u64 v[8:9], v[8:9], 0, v[2:3]
	v_lshl_add_u64 v[8:9], v[8:9], 0, v[4:5]
	global_load_dwordx4 v[140:143], v[8:9], off
	v_cmp_gt_u32_e32 vcc, s6, v7
	v_bitop3_b32 v13, v208, v1, 15 bitop3:0x6c
	v_add_u32_e32 v14, 0x200, v7
	v_cndmask_b32_e64 v12, v6, 0, vcc
	v_lshlrev_b32_e32 v13, 4, v13
	v_add_u32_e32 v208, 4, v208
	v_mov_b32_e32 v7, v14
	v_add3_u32 v189, v12, v2, v13
	v_lshrrev_b32_e32 v2, 12, v7
	v_lshlrev_b32_e32 v10, 11, v208
	v_lshlrev_b64 v[8:9], 16, v[2:3]
	v_and_b32_e32 v2, 0xf800, v10
	v_lshl_add_u64 v[8:9], s[0:1], 0, v[8:9]
	v_lshl_add_u64 v[8:9], v[8:9], 0, v[2:3]
	v_lshl_add_u64 v[8:9], v[8:9], 0, v[4:5]
	global_load_dwordx4 v[144:147], v[8:9], off
	v_cmp_gt_u32_e32 vcc, s6, v7
	v_bitop3_b32 v13, v208, v1, 15 bitop3:0x6c
	v_add_u32_e32 v14, 0x200, v7
	v_cndmask_b32_e64 v12, v6, 0, vcc
	v_lshlrev_b32_e32 v13, 4, v13
	v_add_u32_e32 v208, 4, v208
	v_mov_b32_e32 v7, v14
	v_add3_u32 v190, v12, v2, v13
	v_lshrrev_b32_e32 v2, 12, v7
	v_lshlrev_b32_e32 v10, 11, v208
	v_lshlrev_b64 v[8:9], 16, v[2:3]
	v_and_b32_e32 v2, 0xf800, v10
	v_lshl_add_u64 v[8:9], s[0:1], 0, v[8:9]
	v_lshl_add_u64 v[8:9], v[8:9], 0, v[2:3]
	v_lshl_add_u64 v[8:9], v[8:9], 0, v[4:5]
	global_load_dwordx4 v[148:151], v[8:9], off
	v_cmp_gt_u32_e32 vcc, s6, v7
	v_bitop3_b32 v13, v208, v1, 15 bitop3:0x6c
	v_add_u32_e32 v14, 0x200, v7
	v_cndmask_b32_e64 v12, v6, 0, vcc
	v_lshlrev_b32_e32 v13, 4, v13
	v_add_u32_e32 v208, 4, v208
	v_mov_b32_e32 v7, v14
	v_add3_u32 v191, v12, v2, v13
	v_lshrrev_b32_e32 v2, 12, v7
	v_lshlrev_b32_e32 v10, 11, v208
	v_lshlrev_b64 v[8:9], 16, v[2:3]
	v_and_b32_e32 v2, 0xf800, v10
	v_lshl_add_u64 v[8:9], s[0:1], 0, v[8:9]
	v_lshl_add_u64 v[8:9], v[8:9], 0, v[2:3]
	v_lshl_add_u64 v[8:9], v[8:9], 0, v[4:5]
	global_load_dwordx4 v[152:155], v[8:9], off
	v_cmp_gt_u32_e32 vcc, s6, v7
	v_bitop3_b32 v13, v208, v1, 15 bitop3:0x6c
	v_add_u32_e32 v14, 0x200, v7
	v_cndmask_b32_e64 v12, v6, 0, vcc
	v_lshlrev_b32_e32 v13, 4, v13
	v_add_u32_e32 v208, 4, v208
	v_mov_b32_e32 v7, v14
	v_add3_u32 v192, v12, v2, v13
	v_lshrrev_b32_e32 v2, 12, v7
	v_lshlrev_b32_e32 v10, 11, v208
	v_lshlrev_b64 v[8:9], 16, v[2:3]
	v_and_b32_e32 v2, 0xf800, v10
	v_lshl_add_u64 v[8:9], s[0:1], 0, v[8:9]
; #define LAS __attribute__((address_space(3)))
; __device__ __forceinline__ void p9_router(const Args& a, const Frame& F) {
;     ...
;     for (int i = F.tid; i < 2 * 32 * 128; i += 512) { const int part = i >> 12, r = (i >> 7) & 31, c16 = i & 127;
;         *(LAS u32x4*)((part ? Wlo : Whi) + r * 2048 + ((c16 ^ (r & 15)) << 4)) = *(const u32x4*)(wr + (size_t)part * 32768 + r * 1024 + c16 * 8); }
	v_lshl_add_u64 v[8:9], v[8:9], 0, v[2:3]
	v_lshl_add_u64 v[8:9], v[8:9], 0, v[4:5]
	global_load_dwordx4 v[156:159], v[8:9], off
	v_cmp_gt_u32_e32 vcc, s6, v7
	v_bitop3_b32 v13, v208, v1, 15 bitop3:0x6c
	v_add_u32_e32 v14, 0x200, v7
	v_cndmask_b32_e64 v12, v6, 0, vcc
	v_lshlrev_b32_e32 v13, 4, v13
	v_add_u32_e32 v208, 4, v208
	v_mov_b32_e32 v7, v14
	v_add3_u32 v193, v12, v2, v13
	v_lshrrev_b32_e32 v2, 12, v7
	v_lshlrev_b32_e32 v10, 11, v208
	v_lshlrev_b64 v[8:9], 16, v[2:3]
	v_and_b32_e32 v2, 0xf800, v10
	v_lshl_add_u64 v[8:9], s[0:1], 0, v[8:9]
	v_lshl_add_u64 v[8:9], v[8:9], 0, v[2:3]
	v_lshl_add_u64 v[8:9], v[8:9], 0, v[4:5]
	global_load_dwordx4 v[160:163], v[8:9], off
	v_cmp_gt_u32_e32 vcc, s6, v7
	v_bitop3_b32 v13, v208, v1, 15 bitop3:0x6c
	v_add_u32_e32 v14, 0x200, v7
	v_cndmask_b32_e64 v12, v6, 0, vcc
	v_lshlrev_b32_e32 v13, 4, v13
	v_add_u32_e32 v208, 4, v208
	v_mov_b32_e32 v7, v14
	v_add3_u32 v194, v12, v2, v13
	v_lshrrev_b32_e32 v2, 12, v7
	v_lshlrev_b32_e32 v10, 11, v208
	v_lshlrev_b64 v[8:9], 16, v[2:3]
	v_and_b32_e32 v2, 0xf800, v10
	v_lshl_add_u64 v[8:9], s[0:1], 0, v[8:9]
	v_lshl_add_u64 v[8:9], v[8:9], 0, v[2:3]
	v_lshl_add_u64 v[8:9], v[8:9], 0, v[4:5]
	global_load_dwordx4 v[164:167], v[8:9], off
	v_cmp_gt_u32_e32 vcc, s6, v7
	v_bitop3_b32 v13, v208, v1, 15 bitop3:0x6c
	v_add_u32_e32 v14, 0x200, v7
	v_cndmask_b32_e64 v12, v6, 0, vcc
	v_lshlrev_b32_e32 v13, 4, v13
	v_add_u32_e32 v208, 4, v208
	v_mov_b32_e32 v7, v14
	v_add3_u32 v195, v12, v2, v13
	v_lshrrev_b32_e32 v2, 12, v7
	v_lshlrev_b32_e32 v10, 11, v208
	v_lshlrev_b64 v[8:9], 16, v[2:3]
	v_and_b32_e32 v2, 0xf800, v10
	v_lshl_add_u64 v[8:9], s[0:1], 0, v[8:9]
	v_lshl_add_u64 v[8:9], v[8:9], 0, v[2:3]
	v_lshl_add_u64 v[8:9], v[8:9], 0, v[4:5]
	global_load_dwordx4 v[168:171], v[8:9], off
	v_cmp_gt_u32_e32 vcc, s6, v7
	v_bitop3_b32 v13, v208, v1, 15 bitop3:0x6c
	v_add_u32_e32 v14, 0x200, v7
	v_cndmask_b32_e64 v12, v6, 0, vcc
	v_lshlrev_b32_e32 v13, 4, v13
	v_add_u32_e32 v208, 4, v208
	v_mov_b32_e32 v7, v14
	v_add3_u32 v196, v12, v2, v13
	v_lshrrev_b32_e32 v2, 12, v7
	v_lshlrev_b32_e32 v10, 11, v208
	v_lshlrev_b64 v[8:9], 16, v[2:3]
	v_and_b32_e32 v2, 0xf800, v10
	v_lshl_add_u64 v[8:9], s[0:1], 0, v[8:9]
	v_lshl_add_u64 v[8:9], v[8:9], 0, v[2:3]
	v_lshl_add_u64 v[8:9], v[8:9], 0, v[4:5]
	global_load_dwordx4 v[172:175], v[8:9], off
	v_cmp_gt_u32_e32 vcc, s6, v7
	v_bitop3_b32 v13, v208, v1, 15 bitop3:0x6c
	v_add_u32_e32 v14, 0x200, v7
	v_cndmask_b32_e64 v12, v6, 0, vcc
	v_lshlrev_b32_e32 v13, 4, v13
	v_add_u32_e32 v208, 4, v208
	v_mov_b32_e32 v7, v14
	v_add3_u32 v197, v12, v2, v13
	v_lshrrev_b32_e32 v2, 12, v7
	v_lshlrev_b32_e32 v10, 11, v208
	v_lshlrev_b64 v[8:9], 16, v[2:3]
	v_and_b32_e32 v2, 0xf800, v10
	v_lshl_add_u64 v[8:9], s[0:1], 0, v[8:9]
	v_lshl_add_u64 v[8:9], v[8:9], 0, v[2:3]
	v_lshl_add_u64 v[8:9], v[8:9], 0, v[4:5]
	global_load_dwordx4 v[176:179], v[8:9], off
	v_cmp_gt_u32_e32 vcc, s6, v7
	v_bitop3_b32 v13, v208, v1, 15 bitop3:0x6c
	v_add_u32_e32 v14, 0x200, v7
	v_cndmask_b32_e64 v12, v6, 0, vcc
	v_lshlrev_b32_e32 v13, 4, v13
	v_add_u32_e32 v208, 4, v208
	v_mov_b32_e32 v7, v14
	v_add3_u32 v198, v12, v2, v13
	v_lshrrev_b32_e32 v2, 12, v7
	v_lshlrev_b32_e32 v10, 11, v208
	v_lshlrev_b64 v[8:9], 16, v[2:3]
	v_and_b32_e32 v2, 0xf800, v10
	v_lshl_add_u64 v[8:9], s[0:1], 0, v[8:9]
	v_lshl_add_u64 v[8:9], v[8:9], 0, v[2:3]
	v_lshl_add_u64 v[8:9], v[8:9], 0, v[4:5]
	global_load_dwordx4 v[180:183], v[8:9], off
	v_cmp_gt_u32_e32 vcc, s6, v7
	v_bitop3_b32 v13, v208, v1, 15 bitop3:0x6c
	v_add_u32_e32 v14, 0x200, v7
	v_cndmask_b32_e64 v12, v6, 0, vcc
	v_lshlrev_b32_e32 v13, 4, v13
	v_add_u32_e32 v208, 4, v208
	v_mov_b32_e32 v7, v14
	v_add3_u32 v199, v12, v2, v13
	s_waitcnt vmcnt(0)
	ds_write_b128 v184, v[120:123]
	ds_write_b128 v185, v[124:127]
	ds_write_b128 v186, v[128:131]
	ds_write_b128 v187, v[132:135]
	ds_write_b128 v188, v[136:139]
	ds_write_b128 v189, v[140:143]
	ds_write_b128 v190, v[144:147]
	ds_write_b128 v191, v[148:151]
	ds_write_b128 v192, v[152:155]
	ds_write_b128 v193, v[156:159]
	ds_write_b128 v194, v[160:163]
	ds_write_b128 v195, v[164:167]
	ds_write_b128 v196, v[168:171]
	ds_write_b128 v197, v[172:175]
	ds_write_b128 v198, v[176:179]
	ds_write_b128 v199, v[180:183]
	s_or_b64 exec, exec, s[4:5]
	s_cmpk_gt_i32 s2, 0xff
	s_cbranch_scc1 .LBB0_838
; template <int NT, bool XBF16> ...
;     ...
;     ss += __shfl_xor(ss, 16); ss += __shfl_xor(ss, 32);
;     if (q == 0) red[wave * 16 + c] = ss;
;     LDS_BARRIER();
;     const float rstd = rsqrtf((red[wave * 16 + c] + red[(wave ^ 1) * 16 + c]) * (1.f / 1024.f) + EPS);
;     const LAS f32x4* np = (const LAS f32x4*)nwsL + 128 * hf + 2 * q; const LAS f32x4* hp = (const LAS f32x4*)shL + 128 * hf + 2 * q;
;     const int ln_ = c + 16 * q, pq_ = ln_ & 3, baddr_ = 4 * (((ln_ >> 2) & 15) + 16 * pq_);
;     u32x4* op = (u32x4*)orow + 64 * hf + pq_;
; #pragma unroll
;     for (int j = 0; j < 16; ++j) {
;         const f32x4 y0 = (xa[j] * rstd) * np[j * 8] + hp[j * 8], y1 = (xb[j] * rstd) * np[j * 8 + 1] + hp[j * 8 + 1];
;         u32x4 hi; hi.x = pg8::cvt_pk_bf16(y0.x, y0.y); hi.y = pg8::cvt_pk_bf16(y0.z, y0.w); hi.z = pg8::cvt_pk_bf16(y1.x, y1.y); hi.w = pg8::cvt_pk_bf16(y1.z, y1.w);
;         op[j * 4] = lane_perm(hi, baddr_);
;         u32x4 lo; lo.x = pg8::cvt_pk_bf16(y0.x - bflo(hi.x), y0.y - bfhi(hi.x)); lo.y = pg8::cvt_pk_bf16(y0.z - bflo(hi.y), y0.w - bfhi(hi.y));
;         lo.z = pg8::cvt_pk_bf16(y1.x - bflo(hi.z), y1.y - bfhi(hi.z)); lo.w = pg8::cvt_pk_bf16(y1.z - bflo(hi.w), y1.w - bfhi(hi.w));
;         const bf16x8 ah = __builtin_bit_cast(bf16x8, hi), al = __builtin_bit_cast(bf16x8, lo);
;         const int wo = (((4 * (16 * hf + j) + q) ^ c) << 4);
; #pragma unroll
; __device__ __forceinline__ void p9_router(const Args& a, const Frame& F) {
;     ...
;     const int c = F.lane & 15, q = F.lane >> 4, pair = F.wave >> 1;
;     const float br0 = a.in[IN_BR][c], br1 = a.in[IN_BR][16 + c];
;     for (int chunk = F.bid; chunk < T / 256; chunk += F.G) {
;         const int bidx = (chunk * 256) >> 13;
;         __syncthreads();
;         if (F.tid < 32) hist[F.tid] = 0;
;         for (int k = F.tid; k < 1024; k += 512) { NWS[k] = a.in[IN_N2W][k] * (1.0f + mod[bidx * 6144 + 4096 + k]); SHV[k] = mod[bidx * 6144 + 3072 + k]; }
;         __syncthreads();
;         for (int st = 0; st < 4; ++st) {
;             const int tl0 = (st * 4 + pair) * 16, r = chunk * 256 + tl0 + c;
;             f32x4 acc[2]; acc[0] = (f32x4){0.f, 0.f, 0.f, 0.f}; acc[1] = (f32x4){0.f, 0.f, 0.f, 0.f};
;             norm_pair<2, true>(x1_row(a.out, a.ws, chunk * 256 + tl0 + ((F.lane >> 2) & 15)), NWS, SHV, H2 + (size_t)(chunk * 256 + tl0 + ((F.lane >> 2) & 15)) * D, Whi, Wlo, red, F.wave, c, q, acc);
	v_and_b32_e32 v14, 15, v0
	v_lshlrev_b32_e32 v1, 2, v14
	global_load_dword v19, v1, s[22:23]
	global_load_dword v18, v1, s[22:23] offset:64
	s_add_u32 s24, s72, 0x200000
	s_addc_u32 s25, s73, 0
	s_add_u32 s28, s72, 0x400000
	s_addc_u32 s29, s73, 0
	s_add_u32 s22, s72, 0x100000
	s_addc_u32 s23, s73, 0
	s_add_u32 s38, s72, 0x680000
	s_addc_u32 s39, s73, 0
	s_add_u32 s40, s72, 0x300000
	s_addc_u32 s41, s73, 0
	s_lshr_b32 s4, s94, 7
	s_lshl_b32 s13, s4, 4
	v_mbcnt_lo_u32_b32 v4, -1, 0
	s_bfe_u32 s34, s94, 0x10006
	s_lshl_b32 s4, s4, 10
	v_mbcnt_hi_u32_b32 v4, -1, v4
	s_lshl_b32 s35, s34, 11
	s_add_i32 s4, s4, 0
	v_and_b32_e32 v7, 64, v4
	s_add_i32 s33, 0, 0x22080
	s_add_i32 s36, s35, 0
	s_add_i32 s50, 0, 0x21000
	s_add_i32 s51, s4, 0x22280
	v_xor_b32_e32 v5, 16, v4
	v_add_u32_e32 v7, 64, v7
	s_add_u32 s46, s72, 0x3b200000
	v_cmp_lt_i32_e32 vcc, v5, v7
	s_addc_u32 s47, s73, 0
	s_add_u32 s48, s70, 0x8000000
	v_cndmask_b32_e32 v5, v4, v5, vcc
	v_lshlrev_b32_e32 v45, 2, v5
	v_xor_b32_e32 v5, 32, v4
	s_addc_u32 s49, s71, 0
	s_lshl_b32 s52, s34, 6
	s_and_b32 s54, s94, 0xffffffc0
	s_lshl_b32 s14, s34, 10
	v_lshrrev_b32_e32 v3, 4, v252
	v_cmp_lt_i32_e32 vcc, v5, v7
	s_add_u32 s14, s72, s14
	v_and_b32_e32 v2, 3, v0
	v_cndmask_b32_e32 v4, v4, v5, vcc
	v_add_u32_e32 v7, s33, v1
	v_lshlrev_b32_e32 v1, 5, v3
	s_addc_u32 s15, s73, 0
	s_add_i32 s36, s36, 0x20000
	s_add_i32 s35, s35, s50
	v_mov_b32_e32 v17, 0
	v_lshlrev_b32_e32 v144, 2, v4
	v_and_b32_e32 v4, 60, v0
	v_lshlrev_b32_e32 v16, 4, v2
	v_add_u32_e32 v147, s36, v1
	v_add_u32_e32 v148, s35, v1
	v_or_b32_e32 v1, s52, v3
	v_lshl_or_b32 v145, v2, 6, v4
	v_lshl_add_u64 v[4:5], s[14:15], 0, v[16:17]
	v_bitop3_b32 v16, v1, v14, 16 bitop3:0x36
	v_lshlrev_b32_e32 v16, 4, v16
	v_add_u32_e32 v25, 0, v16
	v_add_u32_e32 v26, s12, v16
	v_bitop3_b32 v16, v1, v14, 20 bitop3:0x36
	v_lshlrev_b32_e32 v16, 4, v16
	v_add_u32_e32 v27, 0, v16
	v_add_u32_e32 v28, s12, v16
	v_bitop3_b32 v16, v1, v14, 24 bitop3:0x36
	v_lshlrev_b32_e32 v16, 4, v16
	v_add_u32_e32 v29, 0, v16
	v_add_u32_e32 v30, s12, v16
	v_bitop3_b32 v16, v1, v14, 28 bitop3:0x36
	v_lshlrev_b32_e32 v16, 4, v16
	v_add_u32_e32 v31, 0, v16
	v_add_u32_e32 v32, s12, v16
	v_bitop3_b32 v16, v1, v14, 32 bitop3:0x36
	v_lshlrev_b32_e32 v16, 4, v16
	v_add_u32_e32 v33, 0, v16
	v_add_u32_e32 v34, s12, v16
	v_bitop3_b32 v16, v1, v14, 36 bitop3:0x36
	v_lshlrev_b32_e32 v16, 4, v16
	v_add_u32_e32 v35, 0, v16
	v_add_u32_e32 v36, s12, v16
	v_bitop3_b32 v16, v1, v14, 40 bitop3:0x36
	v_lshlrev_b32_e32 v16, 4, v16
	v_add_u32_e32 v37, 0, v16
	v_add_u32_e32 v38, s12, v16
	v_bitop3_b32 v16, v1, v14, 44 bitop3:0x36
	v_lshlrev_b32_e32 v16, 4, v16
	v_add_u32_e32 v39, 0, v16
	v_add_u32_e32 v40, s12, v16
	v_bitop3_b32 v16, v1, v14, 48 bitop3:0x36
	v_lshlrev_b32_e32 v16, 4, v16
	v_add_u32_e32 v41, 0, v16
	v_add_u32_e32 v42, s12, v16
	v_bitop3_b32 v16, v1, v14, 52 bitop3:0x36
	s_mov_b64 s[14:15], 0x27200000
	v_lshlrev_b32_e32 v16, 4, v16
	v_lshlrev_b32_e32 v6, 2, v3
	v_lshl_add_u64 v[20:21], v[4:5], 0, s[14:15]
	s_lshl_b32 s14, s96, 4
	v_bitop3_b32 v3, s52, v14, v3 bitop3:0x36
	v_bitop3_b32 v5, v1, v14, 4 bitop3:0x36
	v_bitop3_b32 v11, v1, v14, 8 bitop3:0x36
	v_bitop3_b32 v13, v1, v14, 12 bitop3:0x36
	v_add_u32_e32 v43, 0, v16
	v_add_u32_e32 v44, s12, v16
	v_bitop3_b32 v16, v1, v14, 56 bitop3:0x36
	v_bitop3_b32 v1, v1, v14, 60 bitop3:0x36
	v_bitop3_b32 v4, s14, 16, v14 bitop3:0x36
	v_lshlrev_b32_e32 v3, 4, v3
	v_lshlrev_b32_e32 v5, 4, v5
	v_lshlrev_b32_e32 v11, 4, v11
	v_lshlrev_b32_e32 v13, 4, v13
	v_lshlrev_b32_e32 v16, 4, v16
	v_lshlrev_b32_e32 v1, 4, v1
	v_lshl_add_u32 v146, v4, 2, s33
	v_add_u32_e32 v4, 0, v3
	v_add_u32_e32 v3, s12, v3
	v_add_u32_e32 v10, 0, v5
	v_add_u32_e32 v5, s12, v5
	v_add_u32_e32 v12, 0, v11
	v_add_u32_e32 v11, s12, v11
	v_add_u32_e32 v24, 0, v13
	v_add_u32_e32 v13, s12, v13
	v_add_u32_e32 v47, s12, v16
	v_add_u32_e32 v49, s12, v1
	s_and_b32 s12, 64, s94
	s_cmp_eq_u32 s34, 0
	s_cselect_b64 s[42:43], -1, 0
	s_cmp_lg_u32 s12, 0
	v_add_u32_e32 v46, 0, v16
	s_cselect_b64 s[44:45], -1, 0
	v_lshlrev_b32_e32 v16, 2, v0
	s_add_i32 s12, 0, 0x22000
	v_add_u32_e32 v150, s12, v16
	s_lshl_b32 s12, s2, 8
	v_lshlrev_b32_e32 v8, 11, v14
	v_lshrrev_b32_e32 v9, 2, v0
	v_add_u32_e32 v48, 0, v1
	s_add_i32 s12, s12, s13
	s_mov_b32 s37, 0
	v_lshl_or_b32 v15, v14, 4, v6
	v_cmp_gt_u32_e64 s[0:1], 16, v252
	v_cmp_gt_u32_e64 s[16:17], 4, v14
	v_cmp_eq_u32_e64 s[4:5], 0, v14
	v_cmp_eq_u32_e64 s[6:7], 1, v14
	v_cmp_eq_u32_e64 s[8:9], 2, v14
	v_cmp_gt_u32_e64 s[10:11], 32, v0
	v_lshl_add_u32 v149, v252, 4, s51
	v_mov_b32_e32 v1, v14
	v_lshl_add_u64 v[22:23], s[18:19], 0, v[16:17]
	v_or_b32_e32 v151, 0xfffffe00, v0
	v_add_u32_e32 v152, s50, v16
	v_or_b32_e32 v153, s12, v6
	s_lshl_b32 s50, s3, 8
	v_and_or_b32 v154, v9, 15, s12
	s_mov_b64 s[18:19], 0x800
	s_movk_i32 s51, 0x7800
	s_lshl_b32 s36, s52, 4
	v_lshlrev_b32_e32 v16, 4, v2
	v_mov_b32_e32 v155, 0x358637bd
	s_mov_b32 s52, 0x800000
	v_add_u32_e32 v156, v4, v8
	v_add_u32_e32 v157, v3, v8
	v_add_u32_e32 v158, v10, v8
	v_add_u32_e32 v159, v5, v8
	v_add_u32_e32 v160, v12, v8
	v_add_u32_e32 v161, v11, v8
	v_add_u32_e32 v162, v24, v8
	v_add_u32_e32 v163, v13, v8
	v_add_u32_e32 v164, v25, v8
	v_add_u32_e32 v165, v26, v8
	v_add_u32_e32 v166, v27, v8
	v_add_u32_e32 v167, v28, v8
	v_add_u32_e32 v168, v29, v8
	v_add_u32_e32 v169, v30, v8
	v_add_u32_e32 v170, v31, v8
	v_add_u32_e32 v171, v32, v8
	v_add_u32_e32 v172, v33, v8
	v_add_u32_e32 v173, v34, v8
	v_add_u32_e32 v174, v35, v8
	v_add_u32_e32 v175, v36, v8
	v_add_u32_e32 v176, v37, v8
	v_add_u32_e32 v177, v38, v8
	v_add_u32_e32 v178, v39, v8
	v_add_u32_e32 v179, v40, v8
	v_add_u32_e32 v180, v41, v8
	v_add_u32_e32 v181, v42, v8
	v_add_u32_e32 v182, v43, v8
	v_add_u32_e32 v183, v44, v8
	v_add_u32_e32 v184, v46, v8
	v_add_u32_e32 v185, v47, v8
	v_add_u32_e32 v186, v48, v8
	v_add_u32_e32 v187, v49, v8
	s_movk_i32 s53, 0xffe0
	v_mov_b32_e32 v188, 1
	v_add_u32_e32 v189, s54, v7
	v_bfrev_b32_e32 v190, 1
	s_mov_b32 s54, s2
	s_branch .LBB0_812

; __device__ __forceinline__ void moe_tables(const Args& a, const Frame& F) {
;     ...
;     __syncthreads();
;     for (int i = F.tid; i < 8192; i += 512) tmp[i] = cnt[i];
.LBB0_888:
	s_cmp_lt_i32 s74, 11
	s_cselect_b64 s[4:5], -1, 0
	s_and_b64 s[4:5], s[4:5], s[0:1]
	s_andn2_b64 vcc, exec, s[4:5]
	s_cbranch_vccnz .LBB0_988
	s_add_u32 s0, s72, 0x680000
	s_addc_u32 s1, s73, 0
	v_mov_b32_e32 v5, 0
	v_mov_b32_e32 v4, v0
	v_or_b32_e32 v2, 0x200, v0
	v_lshl_add_u64 v[6:7], v[4:5], 2, s[0:1]
	v_mov_b32_e32 v3, v5
	s_waitcnt vmcnt(0) lgkmcnt(0)
	s_barrier
	v_lshl_add_u64 v[2:3], v[2:3], 2, s[0:1]
	global_load_dword v10, v[6:7], off
	global_load_dword v11, v[2:3], off
	v_or_b32_e32 v3, 0x400, v0
	v_or_b32_e32 v2, 0x600, v0
	v_lshlrev_b32_e32 v3, 2, v3
	v_lshlrev_b32_e32 v2, 2, v2
	global_load_dword v12, v3, s[0:1]
	global_load_dword v13, v2, s[0:1]
	v_or_b32_e32 v3, 0x800, v0
	v_or_b32_e32 v2, 0xa00, v0
	v_lshlrev_b32_e32 v3, 2, v3
	v_lshlrev_b32_e32 v2, 2, v2
	global_load_dword v14, v3, s[0:1]
	global_load_dword v15, v2, s[0:1]
	v_or_b32_e32 v3, 0xc00, v0
	v_or_b32_e32 v2, 0xe00, v0
	v_lshlrev_b32_e32 v3, 2, v3
	v_lshlrev_b32_e32 v2, 2, v2
	global_load_dword v16, v3, s[0:1]
	global_load_dword v17, v2, s[0:1]
	v_or_b32_e32 v3, 0x1000, v0
	v_or_b32_e32 v2, 0x1200, v0
	v_lshlrev_b32_e32 v3, 2, v3
	v_lshlrev_b32_e32 v2, 2, v2
	global_load_dword v18, v3, s[0:1]
	global_load_dword v19, v2, s[0:1]
	v_or_b32_e32 v3, 0x1400, v0
	v_or_b32_e32 v2, 0x1600, v0
	v_lshlrev_b32_e32 v3, 2, v3
	v_lshlrev_b32_e32 v2, 2, v2
	global_load_dword v20, v3, s[0:1]
	global_load_dword v21, v2, s[0:1]
	v_or_b32_e32 v3, 0x1800, v0
	v_or_b32_e32 v2, 0x1a00, v0
	v_lshlrev_b32_e32 v3, 2, v3
	v_lshlrev_b32_e32 v2, 2, v2
	global_load_dword v22, v3, s[0:1]
	global_load_dword v23, v2, s[0:1]
	v_or_b32_e32 v3, 0x1c00, v0
	v_or_b32_e32 v2, 0x1e00, v0
	v_lshlrev_b32_e32 v3, 2, v3
	v_lshlrev_b32_e32 v2, 2, v2
	global_load_dword v24, v3, s[0:1]
	global_load_dword v25, v2, s[0:1]
	s_waitcnt vmcnt(0)
	ds_write2st64_b32 v254, v10, v11 offset1:8
	ds_write2st64_b32 v254, v12, v13 offset0:16 offset1:24
	ds_write2st64_b32 v254, v14, v15 offset0:32 offset1:40
	ds_write2st64_b32 v254, v16, v17 offset0:48 offset1:56
	ds_write2st64_b32 v254, v18, v19 offset0:64 offset1:72
	ds_write2st64_b32 v254, v20, v21 offset0:80 offset1:88
	ds_write2st64_b32 v254, v22, v23 offset0:96 offset1:104
	ds_write2st64_b32 v254, v24, v25 offset0:112 offset1:120
	s_mov_b64 s[6:7], exec
